# proj GEMM K-loop: LDS fragment addresses folded into ds_read immediate offsets and DMA addresses switched to sgpr-base form (no VALU in load phases)
# speedup vs baseline: 1.0055x; 1.0040x over previous
.LBB0_484:
	v_lshrrev_b32_e32 v11, 4, v9
	s_xor_b64 s[18:19], s[2:3], -1
	v_bfe_u32 v11, v11, 1, 1
	s_lshl_b32 s2, s23, 13
	v_lshl_or_b32 v15, v11, 10, s2
	s_lshl_b32 s2, s22, 5
	s_and_b32 s5, s2, 0x60
	s_lshr_b32 s2, s5, 3
	v_or_b32_e32 v11, s2, v11
	s_mov_b64 s[2:3], 0x80
	s_add_i32 m0, s49, 0x18000
	v_lshl_add_u64 v[6:7], v[6:7], 0, s[2:3]
	s_waitcnt vmcnt(2)
	s_barrier
	global_load_lds_dwordx4 v[6:7], off
	v_lshl_add_u64 v[4:5], v[4:5], 0, s[2:3]
	s_add_i32 m0, s49, 0x1a000
	s_add_i32 s65, s49, 0x8000
	global_load_lds_dwordx4 v[4:5], off
	v_lshl_add_u64 v[0:1], v[0:1], 0, s[2:3]
	s_mov_b32 m0, s65
	s_add_i32 s92, s49, 0xa000
	global_load_lds_dwordx4 v[0:1], off
	v_lshl_add_u64 v[0:1], v[2:3], 0, s[2:3]
	s_add_u32 s2, s20, 0x20080
	s_mov_b32 m0, s92
	s_addc_u32 s3, s21, 0
	global_load_lds_dwordx4 v[0:1], off
	s_add_i32 m0, s49, 0x1c000
	v_lshl_add_u64 v[0:1], s[2:3], 0, v[194:195]
	global_load_lds_dwordx4 v[0:1], off
	v_lshl_add_u64 v[0:1], s[2:3], 0, v[196:197]
	s_add_i32 m0, s49, 0x1e000
	s_cmpk_lt_u32 s9, 0x100
	global_load_lds_dwordx4 v[0:1], off
	v_mul_f32_e32 v0, 0x4f7ffffe, v8
	v_cvt_u32_f32_e32 v0, v0
	s_cselect_b64 s[20:21], -1, 0
	s_sub_i32 s2, 0, s15
	v_and_b32_e32 v10, 15, v9
	v_readfirstlane_b32 s3, v0
	v_cvt_f32_u32_e32 v0, s40
	s_mul_i32 s2, s2, s3
	s_mul_hi_u32 s2, s3, s2
	s_add_i32 s2, s3, s2
	v_rcp_iflag_f32_e32 v0, v0
	v_lshlrev_b32_e32 v13, 1, v9
	v_writelane_b32 v254, s2, 12
	s_sub_i32 s2, 0, s40
	v_mul_f32_e32 v0, 0x4f7ffffe, v0
	v_cvt_u32_f32_e32 v0, v0
	v_bfe_u32 v12, v9, 4, 2
	v_lshl_or_b32 v203, s23, 6, v10
	v_and_b32_e32 v13, 32, v13
	v_readfirstlane_b32 s3, v0
	v_lshlrev_b32_e32 v10, 6, v10
	v_lshlrev_b32_e32 v9, 2, v9
	s_mul_i32 s2, s2, s3
	v_or_b32_e32 v14, v10, v13
	v_and_b32_e32 v9, 32, v9
	v_lshlrev_b32_e32 v11, 10, v11
	s_mul_hi_u32 s2, s3, s2
	v_bitop3_b32 v10, v10, v9, v13 bitop3:0x36
	v_bitop3_b32 v205, v11, v14, v9 bitop3:0xf6
	v_or_b32_e32 v13, 16, v14
	v_bitop3_b32 v14, v14, v9, 16 bitop3:0x36
	s_waitcnt vmcnt(6)
	s_add_i32 s47, s3, s2
	v_or_b32_e32 v10, v10, v15
	v_or_b32_e32 v14, v14, v15
	s_add_u32 s46, s70, 0xee00080
	s_mov_b32 s11, s97
	v_bitop3_b32 v237, v13, v11, v9 bitop3:0xde
	v_lshl_or_b32 v238, v12, 3, s5
	s_mov_b32 s93, 0
	s_addc_u32 s9, s71, 0
	v_add_u32_e32 v239, 0, v10
	v_add_u32_e32 v240, 0, v14
	v_mbcnt_lo_u32_b32 v0, -1, 0
	v_mbcnt_hi_u32_b32 v0, -1, v0
	v_and_b32_e32 v0, 16, v0
	v_xor_b32_e32 v239, v239, v0
	v_xor_b32_e32 v240, v240, v0
	v_xor_b32_e32 v205, v205, v0
	v_xor_b32_e32 v237, v237, v0
	v_add_u32_e32 v205, 0x10000, v205
	v_add_u32_e32 v237, 0x10000, v237
	v_mov_b32_e32 v241, v206
	v_mov_b32_e32 v242, v96
	s_mov_b32 s51, s24
	s_barrier
	s_waitcnt vmcnt(0)
	s_branch .LBB0_487

.LBB0_497:
	s_cmpk_eq_i32 s26, 0x300
	s_cselect_b64 s[28:29], -1, 0
	s_add_i32 s23, 0, 0x10000
	s_add_i32 s30, 0, 0x14000
	ds_read_b128 v[8:11], v205
	ds_read_b128 v[12:15], v237
	ds_read_b128 v[24:27], v205 offset:2048
	ds_read_b128 v[28:31], v237 offset:2048
	ds_read_b128 v[0:3], v205 offset:16384
	ds_read_b128 v[4:7], v237 offset:16384
	ds_read_b128 v[16:19], v205 offset:18432
	ds_read_b128 v[20:23], v237 offset:18432
	s_add_i32 m0, s49, 0xc000
	s_add_u32 s30, s46, s26
	s_addc_u32 s31, s9, s27
	s_add_i32 s23, s49, 0xe000
	s_cmpk_lg_i32 s26, 0x300
	ds_read_b128 v[40:43], v239
	ds_read_b128 v[32:35], v239 offset:2048
	ds_read_b128 v[44:47], v240
	ds_read_b128 v[36:39], v240 offset:2048
	ds_read_b128 v[56:59], v239 offset:4096
	ds_read_b128 v[48:51], v239 offset:6144
	ds_read_b128 v[60:63], v240 offset:4096
	ds_read_b128 v[52:55], v240 offset:6144
	global_load_lds_dwordx4 v96, s[30:31]
	s_mov_b32 m0, s23
	s_nop 0
	global_load_lds_dwordx4 v206, s[30:31]
	s_waitcnt vmcnt(8)
	s_waitcnt lgkmcnt(0)
	s_barrier
	s_setprio 1
	s_waitcnt lgkmcnt(0)
	v_mfma_scale_f32_16x16x128_f8f6f4 v[190:193], v[8:15], v[40:47], v[190:193], v226, v225 op_sel_hi:[0,0,0]
	v_mfma_scale_f32_16x16x128_f8f6f4 v[186:189], v[24:31], v[40:47], v[186:189], v226, v225 op_sel_hi:[0,0,0]
	v_mfma_scale_f32_16x16x128_f8f6f4 v[174:177], v[8:15], v[32:39], v[174:177], v226, v225 op_sel_hi:[0,0,0]
	v_mfma_scale_f32_16x16x128_f8f6f4 v[170:173], v[24:31], v[32:39], v[170:173], v226, v225 op_sel_hi:[0,0,0]
	v_mfma_scale_f32_16x16x128_f8f6f4 v[158:161], v[8:15], v[56:63], v[158:161], v226, v225 op_sel_hi:[0,0,0]
	v_mfma_scale_f32_16x16x128_f8f6f4 v[154:157], v[24:31], v[56:63], v[154:157], v226, v225 op_sel_hi:[0,0,0]
	v_mfma_scale_f32_16x16x128_f8f6f4 v[142:145], v[8:15], v[48:55], v[142:145], v226, v225 op_sel_hi:[0,0,0]
	v_mfma_scale_f32_16x16x128_f8f6f4 v[138:141], v[24:31], v[48:55], v[138:141], v226, v225 op_sel_hi:[0,0,0]
	s_setprio 0
	s_setprio 1
	v_mfma_scale_f32_16x16x128_f8f6f4 v[182:185], v[0:7], v[40:47], v[182:185], v226, v225 op_sel_hi:[0,0,0]
	v_mfma_scale_f32_16x16x128_f8f6f4 v[178:181], v[16:23], v[40:47], v[178:181], v226, v225 op_sel_hi:[0,0,0]
	v_mfma_scale_f32_16x16x128_f8f6f4 v[166:169], v[0:7], v[32:39], v[166:169], v226, v225 op_sel_hi:[0,0,0]
	v_mfma_scale_f32_16x16x128_f8f6f4 v[162:165], v[16:23], v[32:39], v[162:165], v226, v225 op_sel_hi:[0,0,0]
	v_mfma_scale_f32_16x16x128_f8f6f4 v[150:153], v[0:7], v[56:63], v[150:153], v226, v225 op_sel_hi:[0,0,0]
	v_mfma_scale_f32_16x16x128_f8f6f4 v[146:149], v[16:23], v[56:63], v[146:149], v226, v225 op_sel_hi:[0,0,0]
	v_mfma_scale_f32_16x16x128_f8f6f4 v[134:137], v[0:7], v[48:55], v[134:137], v226, v225 op_sel_hi:[0,0,0]
	v_mfma_scale_f32_16x16x128_f8f6f4 v[130:133], v[16:23], v[48:55], v[130:133], v226, v225 op_sel_hi:[0,0,0]
	s_setprio 0
	s_barrier
	s_cbranch_scc1 .LBB0_499
	v_mov_b64_e32 v[212:213], v[210:211]
	v_mov_b64_e32 v[214:215], v[208:209]
	v_mov_b32_e32 v206, v210
	v_mov_b32_e32 v96, v208
	v_mov_b32_e32 v204, v243
	v_mov_b32_e32 v202, v224
	v_mov_b32_e32 v241, v210
	v_mov_b32_e32 v242, v208
	s_branch .LBB0_500

.LBB0_500:
	s_and_b64 s[30:31], s[24:25], s[28:29]
	s_add_i32 s23, s5, 2
	s_and_b64 s[28:29], s[28:29], exec
	s_cselect_b32 s96, 0, s23
	s_and_b64 s[28:29], s[30:31], exec
	s_cselect_b32 s28, s52, s4
	s_ashr_i32 s29, s28, 31
	s_lshl_b64 s[30:31], s[96:97], 7
	s_or_b32 s96, s96, 1
	s_lshl_b64 s[34:35], s[28:29], 18
	s_lshl_b64 s[28:29], s[96:97], 7
	s_add_u32 s72, s6, s34
	s_addc_u32 s73, s7, s35
	s_add_u32 s34, s72, s30
	s_addc_u32 s35, s73, s31
	s_mov_b32 m0, s56
	ds_read_b128 v[56:59], v239 offset:16384
	ds_read_b128 v[60:63], v240 offset:16384
	ds_read_b128 v[48:51], v239 offset:18432
	ds_read_b128 v[52:55], v240 offset:18432
	ds_read_b128 v[40:43], v239 offset:20480
	ds_read_b128 v[44:47], v240 offset:20480
	ds_read_b128 v[32:35], v239 offset:22528
	ds_read_b128 v[36:39], v240 offset:22528
	global_load_lds_dwordx4 v194, s[34:35]
	s_mov_b32 m0, s57
	s_nop 0
	global_load_lds_dwordx4 v196, s[34:35]
	s_add_u32 s34, s34, 0x20000
	s_addc_u32 s35, s35, 0
	s_mov_b32 m0, s58
	s_add_u32 s30, s78, s30
	global_load_lds_dwordx4 v194, s[34:35]
	s_mov_b32 m0, s59
	s_addc_u32 s31, s79, s31
	global_load_lds_dwordx4 v196, s[34:35]
	s_mov_b32 m0, s49
	s_nop 0
	global_load_lds_dwordx4 v202, s[30:31]
	s_mov_b32 m0, s60
	s_nop 0
	global_load_lds_dwordx4 v204, s[30:31]
	s_waitcnt vmcnt(8)
	s_waitcnt lgkmcnt(0)
	s_barrier
	s_setprio 1
	s_waitcnt lgkmcnt(0)
	v_mfma_scale_f32_16x16x128_f8f6f4 v[126:129], v[8:15], v[56:63], v[126:129], v226, v225 op_sel_hi:[0,0,0]
	v_mfma_scale_f32_16x16x128_f8f6f4 v[122:125], v[24:31], v[56:63], v[122:125], v226, v225 op_sel_hi:[0,0,0]
	v_mfma_scale_f32_16x16x128_f8f6f4 v[110:113], v[8:15], v[48:55], v[110:113], v226, v225 op_sel_hi:[0,0,0]
	v_mfma_scale_f32_16x16x128_f8f6f4 v[106:109], v[24:31], v[48:55], v[106:109], v226, v225 op_sel_hi:[0,0,0]
	v_mfma_scale_f32_16x16x128_f8f6f4 v[92:95], v[8:15], v[40:47], v[92:95], v226, v225 op_sel_hi:[0,0,0]
	v_mfma_scale_f32_16x16x128_f8f6f4 v[88:91], v[24:31], v[40:47], v[88:91], v226, v225 op_sel_hi:[0,0,0]
	v_mfma_scale_f32_16x16x128_f8f6f4 v[76:79], v[8:15], v[32:39], v[76:79], v226, v225 op_sel_hi:[0,0,0]
	v_mfma_scale_f32_16x16x128_f8f6f4 v[72:75], v[24:31], v[32:39], v[72:75], v226, v225 op_sel_hi:[0,0,0]
	s_setprio 0
	s_setprio 1
	v_mfma_scale_f32_16x16x128_f8f6f4 v[118:121], v[0:7], v[56:63], v[118:121], v226, v225 op_sel_hi:[0,0,0]
	v_mfma_scale_f32_16x16x128_f8f6f4 v[114:117], v[16:23], v[56:63], v[114:117], v226, v225 op_sel_hi:[0,0,0]
	v_mfma_scale_f32_16x16x128_f8f6f4 v[102:105], v[0:7], v[48:55], v[102:105], v226, v225 op_sel_hi:[0,0,0]
	v_mfma_scale_f32_16x16x128_f8f6f4 v[98:101], v[16:23], v[48:55], v[98:101], v226, v225 op_sel_hi:[0,0,0]
	v_mfma_scale_f32_16x16x128_f8f6f4 v[84:87], v[0:7], v[40:47], v[84:87], v226, v225 op_sel_hi:[0,0,0]
	v_mfma_scale_f32_16x16x128_f8f6f4 v[80:83], v[16:23], v[40:47], v[80:83], v226, v225 op_sel_hi:[0,0,0]
	v_mfma_scale_f32_16x16x128_f8f6f4 v[68:71], v[0:7], v[32:39], v[68:71], v226, v225 op_sel_hi:[0,0,0]
	v_mfma_scale_f32_16x16x128_f8f6f4 v[64:67], v[16:23], v[32:39], v[64:67], v226, v225 op_sel_hi:[0,0,0]
	s_setprio 0
	s_barrier
	s_add_i32 s34, 0, 0x18000
	s_add_i32 s35, 0, 0x1c000
	ds_read_b128 v[0:3], v205 offset:32768
	ds_read_b128 v[4:7], v237 offset:32768
	ds_read_b128 v[8:11], v205 offset:34816
	ds_read_b128 v[12:15], v237 offset:34816
	ds_read_b128 v[16:19], v205 offset:49152
	ds_read_b128 v[20:23], v237 offset:49152
	ds_read_b128 v[24:27], v205 offset:51200
	ds_read_b128 v[28:31], v237 offset:51200
	s_mov_b32 m0, s61
	ds_read_b128 v[32:35], v239 offset:32768
	ds_read_b128 v[40:43], v239 offset:34816
	ds_read_b128 v[36:39], v240 offset:32768
	ds_read_b128 v[44:47], v240 offset:34816
	ds_read_b128 v[48:51], v239 offset:36864
	ds_read_b128 v[56:59], v239 offset:38912
	ds_read_b128 v[52:55], v240 offset:36864
	ds_read_b128 v[60:63], v240 offset:38912
	global_load_lds_dwordx4 v214, s[30:31]
	s_mov_b32 m0, s64
	s_nop 0
	global_load_lds_dwordx4 v212, s[30:31]
	s_waitcnt vmcnt(8)
	s_waitcnt lgkmcnt(0)
	s_barrier
	s_setprio 1
	s_waitcnt lgkmcnt(0)
	v_mfma_scale_f32_16x16x128_f8f6f4 v[190:193], v[0:7], v[32:39], v[190:193], v226, v225 op_sel_hi:[0,0,0]
	v_mfma_scale_f32_16x16x128_f8f6f4 v[186:189], v[8:15], v[32:39], v[186:189], v226, v225 op_sel_hi:[0,0,0]
	v_mfma_scale_f32_16x16x128_f8f6f4 v[174:177], v[0:7], v[40:47], v[174:177], v226, v225 op_sel_hi:[0,0,0]
	v_mfma_scale_f32_16x16x128_f8f6f4 v[170:173], v[8:15], v[40:47], v[170:173], v226, v225 op_sel_hi:[0,0,0]
	v_mfma_scale_f32_16x16x128_f8f6f4 v[158:161], v[0:7], v[48:55], v[158:161], v226, v225 op_sel_hi:[0,0,0]
	v_mfma_scale_f32_16x16x128_f8f6f4 v[154:157], v[8:15], v[48:55], v[154:157], v226, v225 op_sel_hi:[0,0,0]
	v_mfma_scale_f32_16x16x128_f8f6f4 v[142:145], v[0:7], v[56:63], v[142:145], v226, v225 op_sel_hi:[0,0,0]
	v_mfma_scale_f32_16x16x128_f8f6f4 v[138:141], v[8:15], v[56:63], v[138:141], v226, v225 op_sel_hi:[0,0,0]
	s_setprio 0
	s_setprio 1
	v_mfma_scale_f32_16x16x128_f8f6f4 v[182:185], v[16:23], v[32:39], v[182:185], v226, v225 op_sel_hi:[0,0,0]
	v_mfma_scale_f32_16x16x128_f8f6f4 v[178:181], v[24:31], v[32:39], v[178:181], v226, v225 op_sel_hi:[0,0,0]
	v_mfma_scale_f32_16x16x128_f8f6f4 v[166:169], v[16:23], v[40:47], v[166:169], v226, v225 op_sel_hi:[0,0,0]
	v_mfma_scale_f32_16x16x128_f8f6f4 v[162:165], v[24:31], v[40:47], v[162:165], v226, v225 op_sel_hi:[0,0,0]
	v_mfma_scale_f32_16x16x128_f8f6f4 v[150:153], v[16:23], v[48:55], v[150:153], v226, v225 op_sel_hi:[0,0,0]
	v_mfma_scale_f32_16x16x128_f8f6f4 v[146:149], v[24:31], v[48:55], v[146:149], v226, v225 op_sel_hi:[0,0,0]
	v_mfma_scale_f32_16x16x128_f8f6f4 v[134:137], v[16:23], v[56:63], v[134:137], v226, v225 op_sel_hi:[0,0,0]
	v_mfma_scale_f32_16x16x128_f8f6f4 v[130:133], v[24:31], v[56:63], v[130:133], v226, v225 op_sel_hi:[0,0,0]
	s_setprio 0
	s_barrier
	s_add_u32 s30, s72, s28
	s_addc_u32 s31, s73, s29
	s_add_i32 s34, s34, s48
	s_mov_b32 m0, s34
	ds_read_b128 v[32:35], v239 offset:49152
	ds_read_b128 v[40:43], v239 offset:51200
	ds_read_b128 v[36:39], v240 offset:49152
	ds_read_b128 v[44:47], v240 offset:51200
	ds_read_b128 v[48:51], v239 offset:53248
	ds_read_b128 v[56:59], v239 offset:55296
	ds_read_b128 v[52:55], v240 offset:53248
	ds_read_b128 v[60:63], v240 offset:55296
	global_load_lds_dwordx4 v194, s[30:31]
	s_add_i32 m0, s34, 0x2000
	s_add_i32 s34, s35, s48
	global_load_lds_dwordx4 v196, s[30:31]
	s_add_u32 s30, s30, 0x20000
	s_addc_u32 s31, s31, 0
	s_mov_b32 m0, s34
	s_nop 0
	global_load_lds_dwordx4 v194, s[30:31]
	s_add_i32 m0, s34, 0x2000
	s_add_u32 s28, s78, s28
	global_load_lds_dwordx4 v196, s[30:31]
	s_addc_u32 s29, s79, s29
	s_mov_b32 m0, s65
	s_nop 0
	global_load_lds_dwordx4 v202, s[28:29]
	s_mov_b32 m0, s92
	s_nop 0
	global_load_lds_dwordx4 v204, s[28:29]
	s_waitcnt vmcnt(8)
	s_waitcnt lgkmcnt(0)
	s_barrier
	s_setprio 1
	s_waitcnt lgkmcnt(0)
	v_mfma_scale_f32_16x16x128_f8f6f4 v[126:129], v[0:7], v[32:39], v[126:129], v226, v225 op_sel_hi:[0,0,0]
	v_mfma_scale_f32_16x16x128_f8f6f4 v[122:125], v[8:15], v[32:39], v[122:125], v226, v225 op_sel_hi:[0,0,0]
	v_mfma_scale_f32_16x16x128_f8f6f4 v[110:113], v[0:7], v[40:47], v[110:113], v226, v225 op_sel_hi:[0,0,0]
	v_mfma_scale_f32_16x16x128_f8f6f4 v[106:109], v[8:15], v[40:47], v[106:109], v226, v225 op_sel_hi:[0,0,0]
	v_mfma_scale_f32_16x16x128_f8f6f4 v[92:95], v[0:7], v[48:55], v[92:95], v226, v225 op_sel_hi:[0,0,0]
	v_mfma_scale_f32_16x16x128_f8f6f4 v[88:91], v[8:15], v[48:55], v[88:91], v226, v225 op_sel_hi:[0,0,0]
	v_mfma_scale_f32_16x16x128_f8f6f4 v[76:79], v[0:7], v[56:63], v[76:79], v226, v225 op_sel_hi:[0,0,0]
	v_mfma_scale_f32_16x16x128_f8f6f4 v[72:75], v[8:15], v[56:63], v[72:75], v226, v225 op_sel_hi:[0,0,0]
	s_setprio 0
	s_setprio 1
	v_mfma_scale_f32_16x16x128_f8f6f4 v[118:121], v[16:23], v[32:39], v[118:121], v226, v225 op_sel_hi:[0,0,0]
	v_mfma_scale_f32_16x16x128_f8f6f4 v[114:117], v[24:31], v[32:39], v[114:117], v226, v225 op_sel_hi:[0,0,0]
	v_mfma_scale_f32_16x16x128_f8f6f4 v[102:105], v[16:23], v[40:47], v[102:105], v226, v225 op_sel_hi:[0,0,0]
	v_mfma_scale_f32_16x16x128_f8f6f4 v[98:101], v[24:31], v[40:47], v[98:101], v226, v225 op_sel_hi:[0,0,0]
	v_mfma_scale_f32_16x16x128_f8f6f4 v[84:87], v[16:23], v[48:55], v[84:87], v226, v225 op_sel_hi:[0,0,0]
	v_mfma_scale_f32_16x16x128_f8f6f4 v[80:83], v[24:31], v[48:55], v[80:83], v226, v225 op_sel_hi:[0,0,0]
	v_mfma_scale_f32_16x16x128_f8f6f4 v[68:71], v[16:23], v[56:63], v[68:71], v226, v225 op_sel_hi:[0,0,0]
	v_mfma_scale_f32_16x16x128_f8f6f4 v[64:67], v[24:31], v[56:63], v[64:67], v226, v225 op_sel_hi:[0,0,0]
	s_setprio 0
	s_barrier
	s_add_u32 s26, s26, 0x100
	s_addc_u32 s27, s27, 0
	s_cmp_gt_u32 s5, 5
	s_cbranch_scc1 .LBB0_502
	s_mov_b32 s5, s23
	s_branch .LBB0_497
